# speedup vs baseline: 1.0645x; 1.0155x over previous
.Lrec_loop:
	s_add_i32 s10, s36, -1
	s_and_b32 s54, s10, 1
	v_lshl_add_u32 v164, s54, 18, v186
	s_bfe_u32 s54, s10, 0x10001
	s_mul_i32 s54, s54, 0x40004000
	s_sleep 10
	buffer_load_dwordx4 v[16:19], v164, s[16:19], 0 offen sc1
	buffer_load_dwordx4 v[20:23], v164, s[16:19], 0 offen offset:1024 sc1
	buffer_load_dwordx4 v[24:27], v164, s[16:19], 0 offen offset:2048 sc1
	buffer_load_dwordx4 v[28:31], v164, s[16:19], 0 offen offset:3072 sc1
	s_lshl_b32 s41, s36, 7
	s_mov_b32 s43, 0
	s_mov_b32 s45, 15
	s_mov_b32 s46, 0
	s_mov_b32 s55, 0
	s_add_i32 s11, s41, 0x80
	v_add_u32_e32 v206, s11, v169
	v_mov_b32_e32 v207, 0
	v_lshlrev_b64 v[206:207], 14, v[206:207]
	v_lshl_add_u64 v[206:207], v[174:175], 0, v[206:207]
	s_lshl_b32 s11, s36, 16
	s_and_b32 s11, s11, 0x10000
	v_add_u32_e32 v173, s11, v170

.Lrec_check:
	s_bitcmp1_b32 s45, 0
	s_cbranch_scc0 .Lrec_chk0_done
	v_xor_b32_e32 v16, s54, v16
	v_xor_b32_e32 v17, s54, v17
	v_xor_b32_e32 v18, s54, v18
	v_xor_b32_e32 v19, s54, v19
	v_or3_b32 v0, v16, v17, v18
	v_bitop3_b32 v0, v0, s39, v19 bitop3:0xc8
	v_cmp_ne_u32_e32 vcc, 0, v0
	s_cmp_lg_u64 vcc, 0
	s_cbranch_scc1 .Lrec_chk0_dirty
	s_bitset0_b32 s45, 0
	s_branch .Lrec_chk0_done

.Lrec_chk0_done:
	s_bitcmp1_b32 s45, 1
	s_cbranch_scc0 .Lrec_chk1_done
	v_xor_b32_e32 v20, s54, v20
	v_xor_b32_e32 v21, s54, v21
	v_xor_b32_e32 v22, s54, v22
	v_xor_b32_e32 v23, s54, v23
	v_or3_b32 v0, v20, v21, v22
	v_bitop3_b32 v0, v0, s39, v23 bitop3:0xc8
	v_cmp_ne_u32_e32 vcc, 0, v0
	s_cmp_lg_u64 vcc, 0
	s_cbranch_scc1 .Lrec_chk1_dirty
	s_bitset0_b32 s45, 1
	s_branch .Lrec_chk1_done

.Lrec_chk1_done:
	s_bitcmp1_b32 s45, 2
	s_cbranch_scc0 .Lrec_chk2_done
	v_xor_b32_e32 v24, s54, v24
	v_xor_b32_e32 v25, s54, v25
	v_xor_b32_e32 v26, s54, v26
	v_xor_b32_e32 v27, s54, v27
	v_or3_b32 v0, v24, v25, v26
	v_bitop3_b32 v0, v0, s39, v27 bitop3:0xc8
	v_cmp_ne_u32_e32 vcc, 0, v0
	s_cmp_lg_u64 vcc, 0
	s_cbranch_scc1 .Lrec_chk2_dirty
	s_bitset0_b32 s45, 2
	s_branch .Lrec_chk2_done

.Lrec_chk2_done:
	s_bitcmp1_b32 s45, 3
	s_cbranch_scc0 .Lrec_chk3_done
	v_xor_b32_e32 v28, s54, v28
	v_xor_b32_e32 v29, s54, v29
	v_xor_b32_e32 v30, s54, v30
	v_xor_b32_e32 v31, s54, v31
	v_or3_b32 v0, v28, v29, v30
	v_bitop3_b32 v0, v0, s39, v31 bitop3:0xc8
	v_cmp_ne_u32_e32 vcc, 0, v0
	s_cmp_lg_u64 vcc, 0
	s_cbranch_scc1 .Lrec_chk3_dirty
	s_bitset0_b32 s45, 3
	s_branch .Lrec_chk3_done

.Lrec_stall:
	s_and_b64 vcc, exec, s[8:9]
	s_cbranch_vccnz .Lrec_giveup
	s_add_i32 s43, s43, 1
	s_cmp_lt_u32 s43, s38
	s_cbranch_scc0 .Lrec_dead
	s_sleep 2
	s_branch .Lrec_wait

.Lrec_ldone:
	s_cmp_eq_u32 s55, 1
	s_cbranch_scc1 .Lrec_wdone
	v_add_u32_e32 v197, v173, v188
	ds_write_b128 v197, v[198:201] offset:1024
	v_add_u32_e32 v197, v173, v189
	ds_write_b128 v197, v[202:205] offset:2048
	v_add_u32_e32 v197, v173, v190
	ds_write_b128 v197, v[212:215] offset:3072
	v_add_u32_e32 v197, v173, v194
	ds_write_b128 v197, v[216:219] offset:4096
	v_add_u32_e32 v197, v173, v191
	ds_write_b128 v197, v[220:223] offset:5120
	v_add_u32_e32 v197, v173, v192
	ds_write_b128 v197, v[224:227] offset:6144
	v_add_u32_e32 v197, v173, v193
	ds_write_b128 v197, v[228:231] offset:7168
.Lrec_wdone:
	v_add_u32_e32 v173, v173, v187
	s_waitcnt lgkmcnt(0)
	s_barrier
	ds_read_b128 v[0:3], v173 offset:1024
	ds_read_b128 v[4:7], v173 offset:2048
	ds_read_b128 v[8:11], v173 offset:3072
	ds_read_b128 v[12:15], v173 offset:4096
	ds_read_b128 v[16:19], v173 offset:5120
	ds_read_b128 v[20:23], v173 offset:6144
	ds_read_b128 v[24:27], v173 offset:7168
	s_waitcnt lgkmcnt(6)
	v_pk_add_f32 v[234:235], v[234:235], v[2:3]
	v_pk_add_f32 v[232:233], v[232:233], v[0:1]
	s_waitcnt lgkmcnt(5)
	v_pk_add_f32 v[234:235], v[234:235], v[6:7]
	v_pk_add_f32 v[232:233], v[232:233], v[4:5]
	s_waitcnt lgkmcnt(4)
	v_pk_add_f32 v[234:235], v[234:235], v[10:11]
	v_pk_add_f32 v[232:233], v[232:233], v[8:9]
	s_waitcnt lgkmcnt(3)
	v_pk_add_f32 v[234:235], v[234:235], v[14:15]
	v_pk_add_f32 v[232:233], v[232:233], v[12:13]
	s_waitcnt lgkmcnt(2)
	v_pk_add_f32 v[234:235], v[234:235], v[18:19]
	v_pk_add_f32 v[232:233], v[232:233], v[16:17]
	s_waitcnt lgkmcnt(1)
	v_pk_add_f32 v[234:235], v[234:235], v[22:23]
	v_pk_add_f32 v[232:233], v[232:233], v[20:21]
	s_waitcnt lgkmcnt(0)
	v_pk_add_f32 v[18:19], v[234:235], v[26:27]
	v_pk_add_f32 v[16:17], v[232:233], v[24:25]
	v_mul_f32_e32 v16, 0xbfb8aa3b, v16
	v_exp_f32_e32 v20, v16
	v_add_f32_e32 v16, v18, v18
	v_mul_f32_e32 v16, 0x3fb8aa3b, v16
	v_mul_f32_e32 v17, 0xbfb8aa3b, v17
	v_exp_f32_e32 v18, v16
	v_exp_f32_e32 v17, v17
	v_add_f32_e32 v18, 1.0, v18
	v_add_f32_e32 v16, 1.0, v17
	v_add_f32_e32 v17, 1.0, v20
	v_rcp_f32_e32 v18, v18
	v_rcp_f32_e32 v16, v16
	v_rcp_f32_e32 v173, v17
	v_fma_f32 v17, v18, -2.0, 1.0
	v_pk_mul_f32 v[16:17], v[172:173], v[16:17]
	s_nop 0
	v_add_f32_e32 v172, v16, v17
	v_add_f32_e32 v17, v172, v172
	v_mul_f32_e32 v17, 0x3fb8aa3b, v17
	v_mul_f32_e32 v16, 0xbfb8aa3b, v19
	v_exp_f32_e32 v17, v17
	v_exp_f32_e32 v16, v16
	v_add_f32_e32 v17, 1.0, v17
	v_add_f32_e32 v16, 1.0, v16
	v_rcp_f32_e32 v17, v17
	v_rcp_f32_e32 v16, v16
	v_fma_f32 v17, v17, -2.0, 1.0
	v_fma_mixlo_f16 v16, v16, v17, 0
	ds_write_b16 v171, v16
	s_and_saveexec_b64 s[10:11], s[4:5]
	s_cbranch_execz .Lrec_pubdone
	ds_read_b64 v[16:17], v195
	s_and_b32 s12, s36, 1
	s_lshl_b32 s12, s12, 18
	v_mov_b32_e32 v18, s12
	v_mov_b32_e32 v19, 0
	v_lshl_add_u64 v[20:21], v[240:241], 0, v[18:19]
	v_add_u32_e32 v18, s41, v185
	v_lshlrev_b64 v[18:19], 11, v[18:19]
	v_lshl_add_u64 v[22:23], v[180:181], 0, v[18:19]
	s_bfe_u32 s12, s36, 0x10001
	s_mul_i32 s12, s12, 0x40004000
	s_and_b64 vcc, exec, s[6:7]
	s_cbranch_vccz .Lrec_pubfast
	s_waitcnt lgkmcnt(0)
	v_or_b32_e32 v18, s12, v16
	v_or_b32_e32 v19, s12, v17
	global_store_dwordx2 v[20:21], v[18:19], off sc1
	global_store_dwordx2 v[22:23], v[16:17], off
	s_branch .Lrec_pubdone

	.amdhsa_kernel _Z15lstm_persistentPKDF16_PKfPDF16_PjS4_S2_S3_
		.amdhsa_group_segment_fixed_size 0
		.amdhsa_private_segment_fixed_size 0
		.amdhsa_kernarg_size 56
		.amdhsa_user_sgpr_count 2
		.amdhsa_user_sgpr_dispatch_ptr 0
		.amdhsa_user_sgpr_queue_ptr 0
		.amdhsa_user_sgpr_kernarg_segment_ptr 1
		.amdhsa_user_sgpr_dispatch_id 0
		.amdhsa_user_sgpr_kernarg_preload_length 0
		.amdhsa_user_sgpr_kernarg_preload_offset 0
		.amdhsa_user_sgpr_private_segment_size 0
		.amdhsa_uses_dynamic_stack 0
		.amdhsa_enable_private_segment 0
		.amdhsa_system_sgpr_workgroup_id_x 1
		.amdhsa_system_sgpr_workgroup_id_y 0
		.amdhsa_system_sgpr_workgroup_id_z 0
		.amdhsa_system_sgpr_workgroup_info 0
		.amdhsa_system_vgpr_workitem_id 0
		.amdhsa_next_free_vgpr 242
		.amdhsa_next_free_sgpr 56
		.amdhsa_accum_offset 244
		.amdhsa_reserve_vcc 1
		.amdhsa_float_round_mode_32 0
		.amdhsa_float_round_mode_16_64 0
		.amdhsa_float_denorm_mode_32 3
		.amdhsa_float_denorm_mode_16_64 3
		.amdhsa_dx10_clamp 1
		.amdhsa_ieee_mode 1
		.amdhsa_fp16_overflow 0
		.amdhsa_tg_split 0
		.amdhsa_exception_fp_ieee_invalid_op 0
		.amdhsa_exception_fp_denorm_src 0
		.amdhsa_exception_fp_ieee_div_zero 0
		.amdhsa_exception_fp_ieee_overflow 0
		.amdhsa_exception_fp_ieee_underflow 0
		.amdhsa_exception_fp_ieee_inexact 0
		.amdhsa_exception_int_div_zero 0
	.end_amdhsa_kernel

amdhsa.kernels:
  - .agpr_count:     0
    .args:
      - .actual_access:  read_only
        .address_space:  global
        .offset:         0
        .size:           8
        .value_kind:     global_buffer
      - .actual_access:  read_only
        .address_space:  global
        .offset:         8
        .size:           8
        .value_kind:     global_buffer
      - .actual_access:  read_only
        .address_space:  global
        .offset:         16
        .size:           8
        .value_kind:     global_buffer
      - .actual_access:  read_only
        .address_space:  global
        .offset:         24
        .size:           8
        .value_kind:     global_buffer
      - .actual_access:  read_only
        .address_space:  global
        .offset:         32
        .size:           8
        .value_kind:     global_buffer
      - .actual_access:  read_only
        .address_space:  global
        .offset:         40
        .size:           8
        .value_kind:     global_buffer
      - .address_space:  global
        .offset:         48
        .size:           8
        .value_kind:     global_buffer
      - .address_space:  global
        .offset:         56
        .size:           8
        .value_kind:     global_buffer
      - .address_space:  global
        .offset:         64
        .size:           8
        .value_kind:     global_buffer
      - .address_space:  global
        .offset:         72
        .size:           8
        .value_kind:     global_buffer
      - .address_space:  global
        .offset:         80
        .size:           8
        .value_kind:     global_buffer
    .group_segment_fixed_size: 0
    .kernarg_segment_align: 8
    .kernarg_segment_size: 88
    .language:       OpenCL C
    .language_version:
      - 2
      - 0
    .max_flat_workgroup_size: 256
    .name:           _Z11prep_kernelPKfPKiS0_S0_S0_S0_PDF16_S3_S3_S3_Pc
    .private_segment_fixed_size: 0
    .sgpr_count:     30
    .sgpr_spill_count: 0
    .symbol:         _Z11prep_kernelPKfPKiS0_S0_S0_S0_PDF16_S3_S3_S3_Pc.kd
    .uniform_work_group_size: 1
    .uses_dynamic_stack: false
    .vgpr_count:     14
    .vgpr_spill_count: 0
    .wavefront_size: 64
  - .agpr_count:     0
    .args:
      - .actual_access:  read_only
        .address_space:  global
        .offset:         0
        .size:           8
        .value_kind:     global_buffer
      - .address_space:  global
        .offset:         8
        .size:           8
        .value_kind:     global_buffer
    .group_segment_fixed_size: 0
    .kernarg_segment_align: 8
    .kernarg_segment_size: 16
    .language:       OpenCL C
    .language_version:
      - 2
      - 0
    .max_flat_workgroup_size: 256
    .name:           _Z7cvt_wfcPKfPDF16_
    .private_segment_fixed_size: 0
    .sgpr_count:     12
    .sgpr_spill_count: 0
    .symbol:         _Z7cvt_wfcPKfPDF16_.kd
    .uniform_work_group_size: 1
    .uses_dynamic_stack: false
    .vgpr_count:     12
    .vgpr_spill_count: 0
    .wavefront_size: 64
  - .agpr_count:     12
    .args:
      - .actual_access:  read_only
        .address_space:  global
        .offset:         0
        .size:           8
        .value_kind:     global_buffer
      - .actual_access:  read_only
        .address_space:  global
        .offset:         8
        .size:           8
        .value_kind:     global_buffer
      - .address_space:  global
        .offset:         16
        .size:           8
        .value_kind:     global_buffer
      - .address_space:  global
        .offset:         24
        .size:           8
        .value_kind:     global_buffer
      - .offset:         32
        .size:           4
        .value_kind:     by_value
    .group_segment_fixed_size: 0
    .kernarg_segment_align: 8
    .kernarg_segment_size: 36
    .language:       OpenCL C
    .language_version:
      - 2
      - 0
    .max_flat_workgroup_size: 256
    .name:           _Z9lstm_stepPKfS0_PDF16_Pfi
    .private_segment_fixed_size: 0
    .sgpr_count:     21
    .sgpr_spill_count: 0
    .symbol:         _Z9lstm_stepPKfS0_PDF16_Pfi.kd
    .uniform_work_group_size: 1
    .uses_dynamic_stack: false
    .vgpr_count:     88
    .vgpr_spill_count: 0
    .wavefront_size: 64
  - .agpr_count:     0
    .args:
      - .actual_access:  read_only
        .address_space:  global
        .offset:         0
        .size:           8
        .value_kind:     global_buffer
      - .actual_access:  read_only
        .address_space:  global
        .offset:         8
        .size:           8
        .value_kind:     global_buffer
      - .address_space:  global
        .offset:         16
        .size:           8
        .value_kind:     global_buffer
      - .address_space:  global
        .offset:         24
        .size:           8
        .value_kind:     global_buffer
      - .address_space:  global
        .offset:         32
        .size:           8
        .value_kind:     global_buffer
      - .actual_access:  read_only
        .address_space:  global
        .offset:         40
        .size:           8
        .value_kind:     global_buffer
      - .address_space:  global
        .offset:         48
        .size:           8
        .value_kind:     global_buffer
    .group_segment_fixed_size: 0
    .kernarg_segment_align: 8
    .kernarg_segment_size: 56
    .language:       OpenCL C
    .language_version:
      - 2
      - 0
    .max_flat_workgroup_size: 512
    .name:           _Z15lstm_persistentPKDF16_PKfPDF16_PjS4_S2_S3_
    .private_segment_fixed_size: 0
    .sgpr_count:     62
    .sgpr_spill_count: 0
    .symbol:         _Z15lstm_persistentPKDF16_PKfPDF16_PjS4_S2_S3_.kd
    .uniform_work_group_size: 1
    .uses_dynamic_stack: false
    .vgpr_count:     242
    .vgpr_spill_count: 0
    .wavefront_size: 64
  - .agpr_count:     0
    .args:
      - .address_space:  global
        .offset:         0
        .size:           8
        .value_kind:     global_buffer
      - .address_space:  global
        .offset:         8
        .size:           8
        .value_kind:     global_buffer
      - .address_space:  global
        .offset:         16
        .size:           8
        .value_kind:     global_buffer
      - .address_space:  global
        .offset:         24
        .size:           8
        .value_kind:     global_buffer
      - .address_space:  global
        .offset:         32
        .size:           8
        .value_kind:     global_buffer
      - .offset:         40
        .size:           4
        .value_kind:     hidden_block_count_x
      - .offset:         44
        .size:           4
        .value_kind:     hidden_block_count_y
      - .offset:         48
        .size:           4
        .value_kind:     hidden_block_count_z
      - .offset:         52
        .size:           2
        .value_kind:     hidden_group_size_x
      - .offset:         54
        .size:           2
        .value_kind:     hidden_group_size_y
      - .offset:         56
        .size:           2
        .value_kind:     hidden_group_size_z
      - .offset:         58
        .size:           2
        .value_kind:     hidden_remainder_x
      - .offset:         60
        .size:           2
        .value_kind:     hidden_remainder_y
      - .offset:         62
        .size:           2
        .value_kind:     hidden_remainder_z
      - .offset:         80
        .size:           8
        .value_kind:     hidden_global_offset_x
      - .offset:         88
        .size:           8
        .value_kind:     hidden_global_offset_y
      - .offset:         96
        .size:           8
        .value_kind:     hidden_global_offset_z
      - .offset:         104
        .size:           2
        .value_kind:     hidden_grid_dims
      - .offset:         160
        .size:           4
        .value_kind:     hidden_dynamic_lds_size
    .group_segment_fixed_size: 0
    .kernarg_segment_align: 8
    .kernarg_segment_size: 296
    .language:       OpenCL C
    .language_version:
      - 2
      - 0
    .max_flat_workgroup_size: 512
    .name:           _Z11gemm_8phaseILi0EEvPKDF16_S1_PfPKfS4_
    .private_segment_fixed_size: 0
    .sgpr_count:     59
    .sgpr_spill_count: 0
    .symbol:         _Z11gemm_8phaseILi0EEvPKDF16_S1_PfPKfS4_.kd
    .uniform_work_group_size: 1
    .uses_dynamic_stack: false
    .vgpr_count:     226
    .vgpr_spill_count: 0
    .wavefront_size: 64
  - .agpr_count:     0
    .args:
      - .address_space:  global
        .offset:         0
        .size:           8
        .value_kind:     global_buffer
      - .address_space:  global
        .offset:         8
        .size:           8
        .value_kind:     global_buffer
      - .address_space:  global
        .offset:         16
        .size:           8
        .value_kind:     global_buffer
      - .address_space:  global
        .offset:         24
        .size:           8
        .value_kind:     global_buffer
      - .address_space:  global
        .offset:         32
        .size:           8
        .value_kind:     global_buffer
      - .offset:         40
        .size:           4
        .value_kind:     hidden_block_count_x
      - .offset:         44
        .size:           4
        .value_kind:     hidden_block_count_y
      - .offset:         48
        .size:           4
        .value_kind:     hidden_block_count_z
      - .offset:         52
        .size:           2
        .value_kind:     hidden_group_size_x
      - .offset:         54
        .size:           2
        .value_kind:     hidden_group_size_y
      - .offset:         56
        .size:           2
        .value_kind:     hidden_group_size_z
      - .offset:         58
        .size:           2
        .value_kind:     hidden_remainder_x
      - .offset:         60
        .size:           2
        .value_kind:     hidden_remainder_y
      - .offset:         62
        .size:           2
        .value_kind:     hidden_remainder_z
      - .offset:         80
        .size:           8
        .value_kind:     hidden_global_offset_x
      - .offset:         88
        .size:           8
        .value_kind:     hidden_global_offset_y
      - .offset:         96
        .size:           8
        .value_kind:     hidden_global_offset_z
      - .offset:         104
        .size:           2
        .value_kind:     hidden_grid_dims
      - .offset:         160
        .size:           4
        .value_kind:     hidden_dynamic_lds_size
    .group_segment_fixed_size: 0
    .kernarg_segment_align: 8
    .kernarg_segment_size: 296
    .language:       OpenCL C
    .language_version:
      - 2
      - 0
    .max_flat_workgroup_size: 512
    .name:           _Z11gemm_8phaseILi1EEvPKDF16_S1_PfPKfS4_
    .private_segment_fixed_size: 0
    .sgpr_count:     44
    .sgpr_spill_count: 0
    .symbol:         _Z11gemm_8phaseILi1EEvPKDF16_S1_PfPKfS4_.kd
    .uniform_work_group_size: 1
    .uses_dynamic_stack: false
    .vgpr_count:     234
    .vgpr_spill_count: 0
    .wavefront_size: 64
